# hyena third filter layer: forward and backward accumulators as register pairs, one v_pk_fma_f32 per pair (same fused op, same order)
# speedup vs baseline: 1.0007x; 1.0007x over previous
;     ...
;     float asum = 0.f;
; #pragma unroll 1
;     for (int hp = 0; hp < 2; ++hp) {
;         float accf[16], accb[16];
; #pragma unroll
;         for (int i = 0; i < 16; ++i) { accf[i] = 0.f; accb[i] = 0.f; }
; #pragma unroll 2
;         for (int k4 = 0; k4 < 16; ++k4) {
;             float wf[4], wb[4];
; #pragma unroll
;             for (int j = 0; j < 4; ++j) { wf[j] = w3[(k4 * 4 + j) * 1024 + tid]; wb[j] = w3[(k4 * 4 + j) * 1024 + 512 + tid]; }
; #pragma unroll
;             for (int pp = 0; pp < 16; ++pp) {
;                 const float4 hv = *(const float4*)&h2[(hp * 16 + pp) * 64 + k4 * 4];
;                 accf[pp] += hv.x * wf[0]; accf[pp] += hv.y * wf[1]; accf[pp] += hv.z * wf[2]; accf[pp] += hv.w * wf[3];
;                 accb[pp] += hv.x * wb[0]; accb[pp] += hv.y * wb[1]; accb[pp] += hv.z * wb[2]; accb[pp] += hv.w * wb[3];
;             }
;         }
.LBB0_76:
	v_lshlrev_b32_e32 v62, 2, v0
	v_readlane_b32 s98, v253, 59
	v_readlane_b32 s99, v253, 60
	s_mov_b32 s101, s2
	s_mov_b32 s100, 0
	v_mov_b32_e32 v204, 0
	v_mov_b32_e32 v205, 0
	v_mov_b32_e32 v206, 0
	v_mov_b32_e32 v207, 0
	v_mov_b32_e32 v208, 0
	v_mov_b32_e32 v209, 0
	v_mov_b32_e32 v210, 0
	v_mov_b32_e32 v211, 0
	v_mov_b32_e32 v212, 0
	v_mov_b32_e32 v213, 0
	v_mov_b32_e32 v214, 0
	v_mov_b32_e32 v215, 0
	v_mov_b32_e32 v216, 0
	v_mov_b32_e32 v217, 0
	v_mov_b32_e32 v218, 0
	v_mov_b32_e32 v219, 0
	v_mov_b32_e32 v220, 0
	v_mov_b32_e32 v221, 0
	v_mov_b32_e32 v222, 0
	v_mov_b32_e32 v223, 0
	v_mov_b32_e32 v224, 0
	v_mov_b32_e32 v225, 0
	v_mov_b32_e32 v226, 0
	v_mov_b32_e32 v227, 0
	v_mov_b32_e32 v228, 0
	v_mov_b32_e32 v229, 0
	v_mov_b32_e32 v230, 0
	v_mov_b32_e32 v231, 0
	v_mov_b32_e32 v232, 0
	v_mov_b32_e32 v233, 0
	v_mov_b32_e32 v234, 0
	v_mov_b32_e32 v235, 0
	global_load_dword v78, v62, s[98:99]
	global_load_dword v79, v62, s[98:99] offset:2048
	s_add_u32 s98, s98, 0x1000
	s_addc_u32 s99, s99, 0
	global_load_dword v80, v62, s[98:99]
	global_load_dword v81, v62, s[98:99] offset:2048
	s_add_u32 s98, s98, 0x1000
	s_addc_u32 s99, s99, 0
	global_load_dword v82, v62, s[98:99]
	global_load_dword v83, v62, s[98:99] offset:2048
	s_add_u32 s98, s98, 0x1000
	s_addc_u32 s99, s99, 0
	global_load_dword v84, v62, s[98:99]
	global_load_dword v85, v62, s[98:99] offset:2048
	s_add_u32 s98, s98, 0x1000
	s_addc_u32 s99, s99, 0
.Lhy_loop:
	global_load_dword v86, v62, s[98:99]
	global_load_dword v87, v62, s[98:99] offset:2048
	s_add_u32 s98, s98, 0x1000
	s_addc_u32 s99, s99, 0
	global_load_dword v88, v62, s[98:99]
	global_load_dword v89, v62, s[98:99] offset:2048
	s_add_u32 s98, s98, 0x1000
	s_addc_u32 s99, s99, 0
	global_load_dword v90, v62, s[98:99]
	global_load_dword v91, v62, s[98:99] offset:2048
	s_add_u32 s98, s98, 0x1000
	s_addc_u32 s99, s99, 0
	global_load_dword v92, v62, s[98:99]
	global_load_dword v93, v62, s[98:99] offset:2048
	s_add_u32 s98, s98, 0x1000
	s_addc_u32 s99, s99, 0
	v_mov_b32_e32 v63, s101
	s_add_i32 s101, s101, 16
	ds_read_b128 v[94:97], v63
	ds_read_b128 v[98:101], v63 offset:256
	s_waitcnt vmcnt(8)
	ds_read_b128 v[58:61], v63 offset:512
	s_waitcnt lgkmcnt(2)
	v_pk_fma_f32 v[204:205], v[78:79], v[94:95], v[204:205] op_sel:[0,0,0] op_sel_hi:[1,0,1]
	v_pk_fma_f32 v[204:205], v[80:81], v[94:95], v[204:205] op_sel:[0,1,0] op_sel_hi:[1,1,1]
	v_pk_fma_f32 v[204:205], v[82:83], v[96:97], v[204:205] op_sel:[0,0,0] op_sel_hi:[1,0,1]
	v_pk_fma_f32 v[204:205], v[84:85], v[96:97], v[204:205] op_sel:[0,1,0] op_sel_hi:[1,1,1]
	ds_read_b128 v[94:97], v63 offset:768
	s_waitcnt lgkmcnt(2)
	v_pk_fma_f32 v[206:207], v[78:79], v[98:99], v[206:207] op_sel:[0,0,0] op_sel_hi:[1,0,1]
	v_pk_fma_f32 v[206:207], v[80:81], v[98:99], v[206:207] op_sel:[0,1,0] op_sel_hi:[1,1,1]
	v_pk_fma_f32 v[206:207], v[82:83], v[100:101], v[206:207] op_sel:[0,0,0] op_sel_hi:[1,0,1]
	v_pk_fma_f32 v[206:207], v[84:85], v[100:101], v[206:207] op_sel:[0,1,0] op_sel_hi:[1,1,1]
	ds_read_b128 v[98:101], v63 offset:1024
	s_waitcnt lgkmcnt(2)
	v_pk_fma_f32 v[208:209], v[78:79], v[58:59], v[208:209] op_sel:[0,0,0] op_sel_hi:[1,0,1]
	v_pk_fma_f32 v[208:209], v[80:81], v[58:59], v[208:209] op_sel:[0,1,0] op_sel_hi:[1,1,1]
	v_pk_fma_f32 v[208:209], v[82:83], v[60:61], v[208:209] op_sel:[0,0,0] op_sel_hi:[1,0,1]
	v_pk_fma_f32 v[208:209], v[84:85], v[60:61], v[208:209] op_sel:[0,1,0] op_sel_hi:[1,1,1]
	ds_read_b128 v[58:61], v63 offset:1280
	s_waitcnt lgkmcnt(2)
	v_pk_fma_f32 v[210:211], v[78:79], v[94:95], v[210:211] op_sel:[0,0,0] op_sel_hi:[1,0,1]
	v_pk_fma_f32 v[210:211], v[80:81], v[94:95], v[210:211] op_sel:[0,1,0] op_sel_hi:[1,1,1]
	v_pk_fma_f32 v[210:211], v[82:83], v[96:97], v[210:211] op_sel:[0,0,0] op_sel_hi:[1,0,1]
	v_pk_fma_f32 v[210:211], v[84:85], v[96:97], v[210:211] op_sel:[0,1,0] op_sel_hi:[1,1,1]
	ds_read_b128 v[94:97], v63 offset:1536
	s_waitcnt lgkmcnt(2)
	v_pk_fma_f32 v[212:213], v[78:79], v[98:99], v[212:213] op_sel:[0,0,0] op_sel_hi:[1,0,1]
	v_pk_fma_f32 v[212:213], v[80:81], v[98:99], v[212:213] op_sel:[0,1,0] op_sel_hi:[1,1,1]
	v_pk_fma_f32 v[212:213], v[82:83], v[100:101], v[212:213] op_sel:[0,0,0] op_sel_hi:[1,0,1]
	v_pk_fma_f32 v[212:213], v[84:85], v[100:101], v[212:213] op_sel:[0,1,0] op_sel_hi:[1,1,1]
	ds_read_b128 v[98:101], v63 offset:1792
	s_waitcnt lgkmcnt(2)
	v_pk_fma_f32 v[214:215], v[78:79], v[58:59], v[214:215] op_sel:[0,0,0] op_sel_hi:[1,0,1]
	v_pk_fma_f32 v[214:215], v[80:81], v[58:59], v[214:215] op_sel:[0,1,0] op_sel_hi:[1,1,1]
	v_pk_fma_f32 v[214:215], v[82:83], v[60:61], v[214:215] op_sel:[0,0,0] op_sel_hi:[1,0,1]
	v_pk_fma_f32 v[214:215], v[84:85], v[60:61], v[214:215] op_sel:[0,1,0] op_sel_hi:[1,1,1]
	ds_read_b128 v[58:61], v63 offset:2048
	s_waitcnt lgkmcnt(2)
	v_pk_fma_f32 v[216:217], v[78:79], v[94:95], v[216:217] op_sel:[0,0,0] op_sel_hi:[1,0,1]
	v_pk_fma_f32 v[216:217], v[80:81], v[94:95], v[216:217] op_sel:[0,1,0] op_sel_hi:[1,1,1]
	v_pk_fma_f32 v[216:217], v[82:83], v[96:97], v[216:217] op_sel:[0,0,0] op_sel_hi:[1,0,1]
	v_pk_fma_f32 v[216:217], v[84:85], v[96:97], v[216:217] op_sel:[0,1,0] op_sel_hi:[1,1,1]
	ds_read_b128 v[94:97], v63 offset:2304
	s_waitcnt lgkmcnt(2)
	v_pk_fma_f32 v[218:219], v[78:79], v[98:99], v[218:219] op_sel:[0,0,0] op_sel_hi:[1,0,1]
	v_pk_fma_f32 v[218:219], v[80:81], v[98:99], v[218:219] op_sel:[0,1,0] op_sel_hi:[1,1,1]
	v_pk_fma_f32 v[218:219], v[82:83], v[100:101], v[218:219] op_sel:[0,0,0] op_sel_hi:[1,0,1]
	v_pk_fma_f32 v[218:219], v[84:85], v[100:101], v[218:219] op_sel:[0,1,0] op_sel_hi:[1,1,1]
	ds_read_b128 v[98:101], v63 offset:2560
	s_waitcnt lgkmcnt(2)
;     ...
;         for (int k4 = 0; k4 < 16; ++k4) {
;             float wf[4], wb[4];
; #pragma unroll
;             for (int j = 0; j < 4; ++j) { wf[j] = w3[(k4 * 4 + j) * 1024 + tid]; wb[j] = w3[(k4 * 4 + j) * 1024 + 512 + tid]; }
; #pragma unroll
;             for (int pp = 0; pp < 16; ++pp) {
;                 const float4 hv = *(const float4*)&h2[(hp * 16 + pp) * 64 + k4 * 4];
;                 accf[pp] += hv.x * wf[0]; accf[pp] += hv.y * wf[1]; accf[pp] += hv.z * wf[2]; accf[pp] += hv.w * wf[3];
;                 accb[pp] += hv.x * wb[0]; accb[pp] += hv.y * wb[1]; accb[pp] += hv.z * wb[2]; accb[pp] += hv.w * wb[3];
;             }
;         }
	v_pk_fma_f32 v[220:221], v[78:79], v[58:59], v[220:221] op_sel:[0,0,0] op_sel_hi:[1,0,1]
	v_pk_fma_f32 v[220:221], v[80:81], v[58:59], v[220:221] op_sel:[0,1,0] op_sel_hi:[1,1,1]
	v_pk_fma_f32 v[220:221], v[82:83], v[60:61], v[220:221] op_sel:[0,0,0] op_sel_hi:[1,0,1]
	v_pk_fma_f32 v[220:221], v[84:85], v[60:61], v[220:221] op_sel:[0,1,0] op_sel_hi:[1,1,1]
	ds_read_b128 v[58:61], v63 offset:2816
	s_waitcnt lgkmcnt(2)
	v_pk_fma_f32 v[222:223], v[78:79], v[94:95], v[222:223] op_sel:[0,0,0] op_sel_hi:[1,0,1]
	v_pk_fma_f32 v[222:223], v[80:81], v[94:95], v[222:223] op_sel:[0,1,0] op_sel_hi:[1,1,1]
	v_pk_fma_f32 v[222:223], v[82:83], v[96:97], v[222:223] op_sel:[0,0,0] op_sel_hi:[1,0,1]
	v_pk_fma_f32 v[222:223], v[84:85], v[96:97], v[222:223] op_sel:[0,1,0] op_sel_hi:[1,1,1]
	ds_read_b128 v[94:97], v63 offset:3072
	s_waitcnt lgkmcnt(2)
	v_pk_fma_f32 v[224:225], v[78:79], v[98:99], v[224:225] op_sel:[0,0,0] op_sel_hi:[1,0,1]
	v_pk_fma_f32 v[224:225], v[80:81], v[98:99], v[224:225] op_sel:[0,1,0] op_sel_hi:[1,1,1]
	v_pk_fma_f32 v[224:225], v[82:83], v[100:101], v[224:225] op_sel:[0,0,0] op_sel_hi:[1,0,1]
	v_pk_fma_f32 v[224:225], v[84:85], v[100:101], v[224:225] op_sel:[0,1,0] op_sel_hi:[1,1,1]
	ds_read_b128 v[98:101], v63 offset:3328
	s_waitcnt lgkmcnt(2)
	v_pk_fma_f32 v[226:227], v[78:79], v[58:59], v[226:227] op_sel:[0,0,0] op_sel_hi:[1,0,1]
	v_pk_fma_f32 v[226:227], v[80:81], v[58:59], v[226:227] op_sel:[0,1,0] op_sel_hi:[1,1,1]
	v_pk_fma_f32 v[226:227], v[82:83], v[60:61], v[226:227] op_sel:[0,0,0] op_sel_hi:[1,0,1]
	v_pk_fma_f32 v[226:227], v[84:85], v[60:61], v[226:227] op_sel:[0,1,0] op_sel_hi:[1,1,1]
	ds_read_b128 v[58:61], v63 offset:3584
	s_waitcnt lgkmcnt(2)
	v_pk_fma_f32 v[228:229], v[78:79], v[94:95], v[228:229] op_sel:[0,0,0] op_sel_hi:[1,0,1]
	v_pk_fma_f32 v[228:229], v[80:81], v[94:95], v[228:229] op_sel:[0,1,0] op_sel_hi:[1,1,1]
	v_pk_fma_f32 v[228:229], v[82:83], v[96:97], v[228:229] op_sel:[0,0,0] op_sel_hi:[1,0,1]
	v_pk_fma_f32 v[228:229], v[84:85], v[96:97], v[228:229] op_sel:[0,1,0] op_sel_hi:[1,1,1]
	ds_read_b128 v[94:97], v63 offset:3840
	s_waitcnt lgkmcnt(2)
	v_pk_fma_f32 v[230:231], v[78:79], v[98:99], v[230:231] op_sel:[0,0,0] op_sel_hi:[1,0,1]
	v_pk_fma_f32 v[230:231], v[80:81], v[98:99], v[230:231] op_sel:[0,1,0] op_sel_hi:[1,1,1]
	v_pk_fma_f32 v[230:231], v[82:83], v[100:101], v[230:231] op_sel:[0,0,0] op_sel_hi:[1,0,1]
	v_pk_fma_f32 v[230:231], v[84:85], v[100:101], v[230:231] op_sel:[0,1,0] op_sel_hi:[1,1,1]
	s_waitcnt lgkmcnt(1)
	v_pk_fma_f32 v[232:233], v[78:79], v[58:59], v[232:233] op_sel:[0,0,0] op_sel_hi:[1,0,1]
	v_pk_fma_f32 v[232:233], v[80:81], v[58:59], v[232:233] op_sel:[0,1,0] op_sel_hi:[1,1,1]
	v_pk_fma_f32 v[232:233], v[82:83], v[60:61], v[232:233] op_sel:[0,0,0] op_sel_hi:[1,0,1]
	v_pk_fma_f32 v[232:233], v[84:85], v[60:61], v[232:233] op_sel:[0,1,0] op_sel_hi:[1,1,1]
	s_waitcnt lgkmcnt(0)
	v_pk_fma_f32 v[234:235], v[78:79], v[94:95], v[234:235] op_sel:[0,0,0] op_sel_hi:[1,0,1]
	v_pk_fma_f32 v[234:235], v[80:81], v[94:95], v[234:235] op_sel:[0,1,0] op_sel_hi:[1,1,1]
	v_pk_fma_f32 v[234:235], v[82:83], v[96:97], v[234:235] op_sel:[0,0,0] op_sel_hi:[1,0,1]
	v_pk_fma_f32 v[234:235], v[84:85], v[96:97], v[234:235] op_sel:[0,1,0] op_sel_hi:[1,1,1]
	s_cmp_eq_u32 s100, 7
	s_cbranch_scc1 .Lhy_last
	global_load_dword v78, v62, s[98:99]
	global_load_dword v79, v62, s[98:99] offset:2048
	s_add_u32 s98, s98, 0x1000
	s_addc_u32 s99, s99, 0
	global_load_dword v80, v62, s[98:99]
	global_load_dword v81, v62, s[98:99] offset:2048
	s_add_u32 s98, s98, 0x1000
	s_addc_u32 s99, s99, 0
	global_load_dword v82, v62, s[98:99]
	global_load_dword v83, v62, s[98:99] offset:2048
	s_add_u32 s98, s98, 0x1000
	s_addc_u32 s99, s99, 0
	global_load_dword v84, v62, s[98:99]
	global_load_dword v85, v62, s[98:99] offset:2048
	s_add_u32 s98, s98, 0x1000
	s_addc_u32 s99, s99, 0
	v_mov_b32_e32 v63, s101
	s_add_i32 s101, s101, 16
	ds_read_b128 v[94:97], v63
	ds_read_b128 v[98:101], v63 offset:256
	s_waitcnt vmcnt(8)
	ds_read_b128 v[58:61], v63 offset:512
	s_waitcnt lgkmcnt(2)
	v_pk_fma_f32 v[204:205], v[86:87], v[94:95], v[204:205] op_sel:[0,0,0] op_sel_hi:[1,0,1]
	v_pk_fma_f32 v[204:205], v[88:89], v[94:95], v[204:205] op_sel:[0,1,0] op_sel_hi:[1,1,1]
	v_pk_fma_f32 v[204:205], v[90:91], v[96:97], v[204:205] op_sel:[0,0,0] op_sel_hi:[1,0,1]
	v_pk_fma_f32 v[204:205], v[92:93], v[96:97], v[204:205] op_sel:[0,1,0] op_sel_hi:[1,1,1]
	ds_read_b128 v[94:97], v63 offset:768
	s_waitcnt lgkmcnt(2)
	v_pk_fma_f32 v[206:207], v[86:87], v[98:99], v[206:207] op_sel:[0,0,0] op_sel_hi:[1,0,1]
	v_pk_fma_f32 v[206:207], v[88:89], v[98:99], v[206:207] op_sel:[0,1,0] op_sel_hi:[1,1,1]
	v_pk_fma_f32 v[206:207], v[90:91], v[100:101], v[206:207] op_sel:[0,0,0] op_sel_hi:[1,0,1]
	v_pk_fma_f32 v[206:207], v[92:93], v[100:101], v[206:207] op_sel:[0,1,0] op_sel_hi:[1,1,1]
	ds_read_b128 v[98:101], v63 offset:1024
	s_waitcnt lgkmcnt(2)
	v_pk_fma_f32 v[208:209], v[86:87], v[58:59], v[208:209] op_sel:[0,0,0] op_sel_hi:[1,0,1]
	v_pk_fma_f32 v[208:209], v[88:89], v[58:59], v[208:209] op_sel:[0,1,0] op_sel_hi:[1,1,1]
	v_pk_fma_f32 v[208:209], v[90:91], v[60:61], v[208:209] op_sel:[0,0,0] op_sel_hi:[1,0,1]
	v_pk_fma_f32 v[208:209], v[92:93], v[60:61], v[208:209] op_sel:[0,1,0] op_sel_hi:[1,1,1]
	ds_read_b128 v[58:61], v63 offset:1280
	s_waitcnt lgkmcnt(2)
	v_pk_fma_f32 v[210:211], v[86:87], v[94:95], v[210:211] op_sel:[0,0,0] op_sel_hi:[1,0,1]
	v_pk_fma_f32 v[210:211], v[88:89], v[94:95], v[210:211] op_sel:[0,1,0] op_sel_hi:[1,1,1]
	v_pk_fma_f32 v[210:211], v[90:91], v[96:97], v[210:211] op_sel:[0,0,0] op_sel_hi:[1,0,1]
	v_pk_fma_f32 v[210:211], v[92:93], v[96:97], v[210:211] op_sel:[0,1,0] op_sel_hi:[1,1,1]
	ds_read_b128 v[94:97], v63 offset:1536
	s_waitcnt lgkmcnt(2)
;     ...
;         for (int k4 = 0; k4 < 16; ++k4) {
;             float wf[4], wb[4];
; #pragma unroll
;             for (int j = 0; j < 4; ++j) { wf[j] = w3[(k4 * 4 + j) * 1024 + tid]; wb[j] = w3[(k4 * 4 + j) * 1024 + 512 + tid]; }
; #pragma unroll
;             for (int pp = 0; pp < 16; ++pp) {
;                 const float4 hv = *(const float4*)&h2[(hp * 16 + pp) * 64 + k4 * 4];
;                 accf[pp] += hv.x * wf[0]; accf[pp] += hv.y * wf[1]; accf[pp] += hv.z * wf[2]; accf[pp] += hv.w * wf[3];
;                 accb[pp] += hv.x * wb[0]; accb[pp] += hv.y * wb[1]; accb[pp] += hv.z * wb[2]; accb[pp] += hv.w * wb[3];
;             }
;         }
	v_pk_fma_f32 v[212:213], v[86:87], v[98:99], v[212:213] op_sel:[0,0,0] op_sel_hi:[1,0,1]
	v_pk_fma_f32 v[212:213], v[88:89], v[98:99], v[212:213] op_sel:[0,1,0] op_sel_hi:[1,1,1]
	v_pk_fma_f32 v[212:213], v[90:91], v[100:101], v[212:213] op_sel:[0,0,0] op_sel_hi:[1,0,1]
	v_pk_fma_f32 v[212:213], v[92:93], v[100:101], v[212:213] op_sel:[0,1,0] op_sel_hi:[1,1,1]
	ds_read_b128 v[98:101], v63 offset:1792
	s_waitcnt lgkmcnt(2)
	v_pk_fma_f32 v[214:215], v[86:87], v[58:59], v[214:215] op_sel:[0,0,0] op_sel_hi:[1,0,1]
	v_pk_fma_f32 v[214:215], v[88:89], v[58:59], v[214:215] op_sel:[0,1,0] op_sel_hi:[1,1,1]
	v_pk_fma_f32 v[214:215], v[90:91], v[60:61], v[214:215] op_sel:[0,0,0] op_sel_hi:[1,0,1]
	v_pk_fma_f32 v[214:215], v[92:93], v[60:61], v[214:215] op_sel:[0,1,0] op_sel_hi:[1,1,1]
	ds_read_b128 v[58:61], v63 offset:2048
	s_waitcnt lgkmcnt(2)
	v_pk_fma_f32 v[216:217], v[86:87], v[94:95], v[216:217] op_sel:[0,0,0] op_sel_hi:[1,0,1]
	v_pk_fma_f32 v[216:217], v[88:89], v[94:95], v[216:217] op_sel:[0,1,0] op_sel_hi:[1,1,1]
	v_pk_fma_f32 v[216:217], v[90:91], v[96:97], v[216:217] op_sel:[0,0,0] op_sel_hi:[1,0,1]
	v_pk_fma_f32 v[216:217], v[92:93], v[96:97], v[216:217] op_sel:[0,1,0] op_sel_hi:[1,1,1]
	ds_read_b128 v[94:97], v63 offset:2304
	s_waitcnt lgkmcnt(2)
	v_pk_fma_f32 v[218:219], v[86:87], v[98:99], v[218:219] op_sel:[0,0,0] op_sel_hi:[1,0,1]
	v_pk_fma_f32 v[218:219], v[88:89], v[98:99], v[218:219] op_sel:[0,1,0] op_sel_hi:[1,1,1]
	v_pk_fma_f32 v[218:219], v[90:91], v[100:101], v[218:219] op_sel:[0,0,0] op_sel_hi:[1,0,1]
	v_pk_fma_f32 v[218:219], v[92:93], v[100:101], v[218:219] op_sel:[0,1,0] op_sel_hi:[1,1,1]
	ds_read_b128 v[98:101], v63 offset:2560
	s_waitcnt lgkmcnt(2)
	v_pk_fma_f32 v[220:221], v[86:87], v[58:59], v[220:221] op_sel:[0,0,0] op_sel_hi:[1,0,1]
	v_pk_fma_f32 v[220:221], v[88:89], v[58:59], v[220:221] op_sel:[0,1,0] op_sel_hi:[1,1,1]
	v_pk_fma_f32 v[220:221], v[90:91], v[60:61], v[220:221] op_sel:[0,0,0] op_sel_hi:[1,0,1]
	v_pk_fma_f32 v[220:221], v[92:93], v[60:61], v[220:221] op_sel:[0,1,0] op_sel_hi:[1,1,1]
	ds_read_b128 v[58:61], v63 offset:2816
	s_waitcnt lgkmcnt(2)
	v_pk_fma_f32 v[222:223], v[86:87], v[94:95], v[222:223] op_sel:[0,0,0] op_sel_hi:[1,0,1]
	v_pk_fma_f32 v[222:223], v[88:89], v[94:95], v[222:223] op_sel:[0,1,0] op_sel_hi:[1,1,1]
	v_pk_fma_f32 v[222:223], v[90:91], v[96:97], v[222:223] op_sel:[0,0,0] op_sel_hi:[1,0,1]
	v_pk_fma_f32 v[222:223], v[92:93], v[96:97], v[222:223] op_sel:[0,1,0] op_sel_hi:[1,1,1]
	ds_read_b128 v[94:97], v63 offset:3072
	s_waitcnt lgkmcnt(2)
	v_pk_fma_f32 v[224:225], v[86:87], v[98:99], v[224:225] op_sel:[0,0,0] op_sel_hi:[1,0,1]
	v_pk_fma_f32 v[224:225], v[88:89], v[98:99], v[224:225] op_sel:[0,1,0] op_sel_hi:[1,1,1]
	v_pk_fma_f32 v[224:225], v[90:91], v[100:101], v[224:225] op_sel:[0,0,0] op_sel_hi:[1,0,1]
	v_pk_fma_f32 v[224:225], v[92:93], v[100:101], v[224:225] op_sel:[0,1,0] op_sel_hi:[1,1,1]
	ds_read_b128 v[98:101], v63 offset:3328
	s_waitcnt lgkmcnt(2)
	v_pk_fma_f32 v[226:227], v[86:87], v[58:59], v[226:227] op_sel:[0,0,0] op_sel_hi:[1,0,1]
	v_pk_fma_f32 v[226:227], v[88:89], v[58:59], v[226:227] op_sel:[0,1,0] op_sel_hi:[1,1,1]
	v_pk_fma_f32 v[226:227], v[90:91], v[60:61], v[226:227] op_sel:[0,0,0] op_sel_hi:[1,0,1]
	v_pk_fma_f32 v[226:227], v[92:93], v[60:61], v[226:227] op_sel:[0,1,0] op_sel_hi:[1,1,1]
	ds_read_b128 v[58:61], v63 offset:3584
	s_waitcnt lgkmcnt(2)
	v_pk_fma_f32 v[228:229], v[86:87], v[94:95], v[228:229] op_sel:[0,0,0] op_sel_hi:[1,0,1]
	v_pk_fma_f32 v[228:229], v[88:89], v[94:95], v[228:229] op_sel:[0,1,0] op_sel_hi:[1,1,1]
	v_pk_fma_f32 v[228:229], v[90:91], v[96:97], v[228:229] op_sel:[0,0,0] op_sel_hi:[1,0,1]
	v_pk_fma_f32 v[228:229], v[92:93], v[96:97], v[228:229] op_sel:[0,1,0] op_sel_hi:[1,1,1]
	ds_read_b128 v[94:97], v63 offset:3840
	s_waitcnt lgkmcnt(2)
	v_pk_fma_f32 v[230:231], v[86:87], v[98:99], v[230:231] op_sel:[0,0,0] op_sel_hi:[1,0,1]
	v_pk_fma_f32 v[230:231], v[88:89], v[98:99], v[230:231] op_sel:[0,1,0] op_sel_hi:[1,1,1]
	v_pk_fma_f32 v[230:231], v[90:91], v[100:101], v[230:231] op_sel:[0,0,0] op_sel_hi:[1,0,1]
	v_pk_fma_f32 v[230:231], v[92:93], v[100:101], v[230:231] op_sel:[0,1,0] op_sel_hi:[1,1,1]
	s_waitcnt lgkmcnt(1)
	v_pk_fma_f32 v[232:233], v[86:87], v[58:59], v[232:233] op_sel:[0,0,0] op_sel_hi:[1,0,1]
	v_pk_fma_f32 v[232:233], v[88:89], v[58:59], v[232:233] op_sel:[0,1,0] op_sel_hi:[1,1,1]
	v_pk_fma_f32 v[232:233], v[90:91], v[60:61], v[232:233] op_sel:[0,0,0] op_sel_hi:[1,0,1]
	v_pk_fma_f32 v[232:233], v[92:93], v[60:61], v[232:233] op_sel:[0,1,0] op_sel_hi:[1,1,1]
	s_waitcnt lgkmcnt(0)
	v_pk_fma_f32 v[234:235], v[86:87], v[94:95], v[234:235] op_sel:[0,0,0] op_sel_hi:[1,0,1]
	v_pk_fma_f32 v[234:235], v[88:89], v[94:95], v[234:235] op_sel:[0,1,0] op_sel_hi:[1,1,1]
	v_pk_fma_f32 v[234:235], v[90:91], v[96:97], v[234:235] op_sel:[0,0,0] op_sel_hi:[1,0,1]
	v_pk_fma_f32 v[234:235], v[92:93], v[96:97], v[234:235] op_sel:[0,1,0] op_sel_hi:[1,1,1]
	s_add_i32 s100, s100, 1
	s_branch .Lhy_loop
;     ...
;         for (int k4 = 0; k4 < 16; ++k4) {
;             float wf[4], wb[4];
; #pragma unroll
;             for (int j = 0; j < 4; ++j) { wf[j] = w3[(k4 * 4 + j) * 1024 + tid]; wb[j] = w3[(k4 * 4 + j) * 1024 + 512 + tid]; }
; #pragma unroll
;             for (int pp = 0; pp < 16; ++pp) {
;                 const float4 hv = *(const float4*)&h2[(hp * 16 + pp) * 64 + k4 * 4];
;                 accf[pp] += hv.x * wf[0]; accf[pp] += hv.y * wf[1]; accf[pp] += hv.z * wf[2]; accf[pp] += hv.w * wf[3];
;                 accb[pp] += hv.x * wb[0]; accb[pp] += hv.y * wb[1]; accb[pp] += hv.z * wb[2]; accb[pp] += hv.w * wb[3];
;             }
;         }
.Lhy_last:
	v_mov_b32_e32 v63, s101
	s_add_i32 s101, s101, 16
	ds_read_b128 v[94:97], v63
	ds_read_b128 v[98:101], v63 offset:256
	s_waitcnt vmcnt(0)
	ds_read_b128 v[58:61], v63 offset:512
	s_waitcnt lgkmcnt(2)
	v_pk_fma_f32 v[204:205], v[86:87], v[94:95], v[204:205] op_sel:[0,0,0] op_sel_hi:[1,0,1]
	v_pk_fma_f32 v[204:205], v[88:89], v[94:95], v[204:205] op_sel:[0,1,0] op_sel_hi:[1,1,1]
	v_pk_fma_f32 v[204:205], v[90:91], v[96:97], v[204:205] op_sel:[0,0,0] op_sel_hi:[1,0,1]
	v_pk_fma_f32 v[204:205], v[92:93], v[96:97], v[204:205] op_sel:[0,1,0] op_sel_hi:[1,1,1]
	ds_read_b128 v[94:97], v63 offset:768
	s_waitcnt lgkmcnt(2)
	v_pk_fma_f32 v[206:207], v[86:87], v[98:99], v[206:207] op_sel:[0,0,0] op_sel_hi:[1,0,1]
	v_pk_fma_f32 v[206:207], v[88:89], v[98:99], v[206:207] op_sel:[0,1,0] op_sel_hi:[1,1,1]
	v_pk_fma_f32 v[206:207], v[90:91], v[100:101], v[206:207] op_sel:[0,0,0] op_sel_hi:[1,0,1]
	v_pk_fma_f32 v[206:207], v[92:93], v[100:101], v[206:207] op_sel:[0,1,0] op_sel_hi:[1,1,1]
	ds_read_b128 v[98:101], v63 offset:1024
	s_waitcnt lgkmcnt(2)
	v_pk_fma_f32 v[208:209], v[86:87], v[58:59], v[208:209] op_sel:[0,0,0] op_sel_hi:[1,0,1]
	v_pk_fma_f32 v[208:209], v[88:89], v[58:59], v[208:209] op_sel:[0,1,0] op_sel_hi:[1,1,1]
	v_pk_fma_f32 v[208:209], v[90:91], v[60:61], v[208:209] op_sel:[0,0,0] op_sel_hi:[1,0,1]
	v_pk_fma_f32 v[208:209], v[92:93], v[60:61], v[208:209] op_sel:[0,1,0] op_sel_hi:[1,1,1]
	ds_read_b128 v[58:61], v63 offset:1280
	s_waitcnt lgkmcnt(2)
	v_pk_fma_f32 v[210:211], v[86:87], v[94:95], v[210:211] op_sel:[0,0,0] op_sel_hi:[1,0,1]
	v_pk_fma_f32 v[210:211], v[88:89], v[94:95], v[210:211] op_sel:[0,1,0] op_sel_hi:[1,1,1]
	v_pk_fma_f32 v[210:211], v[90:91], v[96:97], v[210:211] op_sel:[0,0,0] op_sel_hi:[1,0,1]
	v_pk_fma_f32 v[210:211], v[92:93], v[96:97], v[210:211] op_sel:[0,1,0] op_sel_hi:[1,1,1]
	ds_read_b128 v[94:97], v63 offset:1536
	s_waitcnt lgkmcnt(2)
	v_pk_fma_f32 v[212:213], v[86:87], v[98:99], v[212:213] op_sel:[0,0,0] op_sel_hi:[1,0,1]
	v_pk_fma_f32 v[212:213], v[88:89], v[98:99], v[212:213] op_sel:[0,1,0] op_sel_hi:[1,1,1]
	v_pk_fma_f32 v[212:213], v[90:91], v[100:101], v[212:213] op_sel:[0,0,0] op_sel_hi:[1,0,1]
	v_pk_fma_f32 v[212:213], v[92:93], v[100:101], v[212:213] op_sel:[0,1,0] op_sel_hi:[1,1,1]
	ds_read_b128 v[98:101], v63 offset:1792
	s_waitcnt lgkmcnt(2)
	v_pk_fma_f32 v[214:215], v[86:87], v[58:59], v[214:215] op_sel:[0,0,0] op_sel_hi:[1,0,1]
	v_pk_fma_f32 v[214:215], v[88:89], v[58:59], v[214:215] op_sel:[0,1,0] op_sel_hi:[1,1,1]
	v_pk_fma_f32 v[214:215], v[90:91], v[60:61], v[214:215] op_sel:[0,0,0] op_sel_hi:[1,0,1]
	v_pk_fma_f32 v[214:215], v[92:93], v[60:61], v[214:215] op_sel:[0,1,0] op_sel_hi:[1,1,1]
	ds_read_b128 v[58:61], v63 offset:2048
	s_waitcnt lgkmcnt(2)
	v_pk_fma_f32 v[216:217], v[86:87], v[94:95], v[216:217] op_sel:[0,0,0] op_sel_hi:[1,0,1]
	v_pk_fma_f32 v[216:217], v[88:89], v[94:95], v[216:217] op_sel:[0,1,0] op_sel_hi:[1,1,1]
	v_pk_fma_f32 v[216:217], v[90:91], v[96:97], v[216:217] op_sel:[0,0,0] op_sel_hi:[1,0,1]
	v_pk_fma_f32 v[216:217], v[92:93], v[96:97], v[216:217] op_sel:[0,1,0] op_sel_hi:[1,1,1]
	ds_read_b128 v[94:97], v63 offset:2304
	s_waitcnt lgkmcnt(2)
	v_pk_fma_f32 v[218:219], v[86:87], v[98:99], v[218:219] op_sel:[0,0,0] op_sel_hi:[1,0,1]
	v_pk_fma_f32 v[218:219], v[88:89], v[98:99], v[218:219] op_sel:[0,1,0] op_sel_hi:[1,1,1]
	v_pk_fma_f32 v[218:219], v[90:91], v[100:101], v[218:219] op_sel:[0,0,0] op_sel_hi:[1,0,1]
	v_pk_fma_f32 v[218:219], v[92:93], v[100:101], v[218:219] op_sel:[0,1,0] op_sel_hi:[1,1,1]
	ds_read_b128 v[98:101], v63 offset:2560
	s_waitcnt lgkmcnt(2)
	v_pk_fma_f32 v[220:221], v[86:87], v[58:59], v[220:221] op_sel:[0,0,0] op_sel_hi:[1,0,1]
	v_pk_fma_f32 v[220:221], v[88:89], v[58:59], v[220:221] op_sel:[0,1,0] op_sel_hi:[1,1,1]
	v_pk_fma_f32 v[220:221], v[90:91], v[60:61], v[220:221] op_sel:[0,0,0] op_sel_hi:[1,0,1]
	v_pk_fma_f32 v[220:221], v[92:93], v[60:61], v[220:221] op_sel:[0,1,0] op_sel_hi:[1,1,1]
	ds_read_b128 v[58:61], v63 offset:2816
	s_waitcnt lgkmcnt(2)
	v_pk_fma_f32 v[222:223], v[86:87], v[94:95], v[222:223] op_sel:[0,0,0] op_sel_hi:[1,0,1]
	v_pk_fma_f32 v[222:223], v[88:89], v[94:95], v[222:223] op_sel:[0,1,0] op_sel_hi:[1,1,1]
	v_pk_fma_f32 v[222:223], v[90:91], v[96:97], v[222:223] op_sel:[0,0,0] op_sel_hi:[1,0,1]
	v_pk_fma_f32 v[222:223], v[92:93], v[96:97], v[222:223] op_sel:[0,1,0] op_sel_hi:[1,1,1]
	ds_read_b128 v[94:97], v63 offset:3072
	s_waitcnt lgkmcnt(2)
;     ...
;             for (int pp = 0; pp < 16; ++pp) {
;                 const float4 hv = *(const float4*)&h2[(hp * 16 + pp) * 64 + k4 * 4];
;                 accf[pp] += hv.x * wf[0]; accf[pp] += hv.y * wf[1]; accf[pp] += hv.z * wf[2]; accf[pp] += hv.w * wf[3];
;                 accb[pp] += hv.x * wb[0]; accb[pp] += hv.y * wb[1]; accb[pp] += hv.z * wb[2]; accb[pp] += hv.w * wb[3];
;             }
;         }
; #pragma unroll
;         for (int pp = 0; pp < 16; ++pp) {
;             const int pos = p0 + hp * 16 + pp;
;             const float t = (float)pos / (float)(l - 1);
;             const float win = expf(-t * delta);
;             const float f = accf[pp] * win, b = accb[pp] * win;
;             HF[pos] = f; asum += fabsf(f);
;             if (pos >= 1) { HF[-pos] = b; asum += fabsf(b); }
;         }
;     }
;     ((float*)(P.ws + WS_NORMP))[(size_t)tid * 520 + task] = asum;
	v_pk_fma_f32 v[224:225], v[86:87], v[98:99], v[224:225] op_sel:[0,0,0] op_sel_hi:[1,0,1]
	v_pk_fma_f32 v[224:225], v[88:89], v[98:99], v[224:225] op_sel:[0,1,0] op_sel_hi:[1,1,1]
	v_pk_fma_f32 v[224:225], v[90:91], v[100:101], v[224:225] op_sel:[0,0,0] op_sel_hi:[1,0,1]
	v_pk_fma_f32 v[224:225], v[92:93], v[100:101], v[224:225] op_sel:[0,1,0] op_sel_hi:[1,1,1]
	ds_read_b128 v[98:101], v63 offset:3328
	s_waitcnt lgkmcnt(2)
	v_pk_fma_f32 v[226:227], v[86:87], v[58:59], v[226:227] op_sel:[0,0,0] op_sel_hi:[1,0,1]
	v_pk_fma_f32 v[226:227], v[88:89], v[58:59], v[226:227] op_sel:[0,1,0] op_sel_hi:[1,1,1]
	v_pk_fma_f32 v[226:227], v[90:91], v[60:61], v[226:227] op_sel:[0,0,0] op_sel_hi:[1,0,1]
	v_pk_fma_f32 v[226:227], v[92:93], v[60:61], v[226:227] op_sel:[0,1,0] op_sel_hi:[1,1,1]
	ds_read_b128 v[58:61], v63 offset:3584
	s_waitcnt lgkmcnt(2)
	v_pk_fma_f32 v[228:229], v[86:87], v[94:95], v[228:229] op_sel:[0,0,0] op_sel_hi:[1,0,1]
	v_pk_fma_f32 v[228:229], v[88:89], v[94:95], v[228:229] op_sel:[0,1,0] op_sel_hi:[1,1,1]
	v_pk_fma_f32 v[228:229], v[90:91], v[96:97], v[228:229] op_sel:[0,0,0] op_sel_hi:[1,0,1]
	v_pk_fma_f32 v[228:229], v[92:93], v[96:97], v[228:229] op_sel:[0,1,0] op_sel_hi:[1,1,1]
	ds_read_b128 v[94:97], v63 offset:3840
	s_waitcnt lgkmcnt(2)
	v_pk_fma_f32 v[230:231], v[86:87], v[98:99], v[230:231] op_sel:[0,0,0] op_sel_hi:[1,0,1]
	v_pk_fma_f32 v[230:231], v[88:89], v[98:99], v[230:231] op_sel:[0,1,0] op_sel_hi:[1,1,1]
	v_pk_fma_f32 v[230:231], v[90:91], v[100:101], v[230:231] op_sel:[0,0,0] op_sel_hi:[1,0,1]
	v_pk_fma_f32 v[230:231], v[92:93], v[100:101], v[230:231] op_sel:[0,1,0] op_sel_hi:[1,1,1]
	s_waitcnt lgkmcnt(1)
	v_pk_fma_f32 v[232:233], v[86:87], v[58:59], v[232:233] op_sel:[0,0,0] op_sel_hi:[1,0,1]
	v_pk_fma_f32 v[232:233], v[88:89], v[58:59], v[232:233] op_sel:[0,1,0] op_sel_hi:[1,1,1]
	v_pk_fma_f32 v[232:233], v[90:91], v[60:61], v[232:233] op_sel:[0,0,0] op_sel_hi:[1,0,1]
	v_pk_fma_f32 v[232:233], v[92:93], v[60:61], v[232:233] op_sel:[0,1,0] op_sel_hi:[1,1,1]
	s_waitcnt lgkmcnt(0)
	v_pk_fma_f32 v[234:235], v[86:87], v[94:95], v[234:235] op_sel:[0,0,0] op_sel_hi:[1,0,1]
	v_pk_fma_f32 v[234:235], v[88:89], v[94:95], v[234:235] op_sel:[0,1,0] op_sel_hi:[1,1,1]
	v_pk_fma_f32 v[234:235], v[90:91], v[96:97], v[234:235] op_sel:[0,0,0] op_sel_hi:[1,0,1]
	v_pk_fma_f32 v[234:235], v[92:93], v[96:97], v[234:235] op_sel:[0,1,0] op_sel_hi:[1,1,1]
	v_mov_b32_e32 v54, v204
	v_mov_b32_e32 v56, v205
	v_mov_b32_e32 v55, v206
	v_mov_b32_e32 v57, v207
	v_mov_b32_e32 v50, v208
	v_mov_b32_e32 v52, v209
	v_mov_b32_e32 v51, v210
	v_mov_b32_e32 v53, v211
	v_mov_b32_e32 v46, v212
	v_mov_b32_e32 v48, v213
	v_mov_b32_e32 v47, v214
	v_mov_b32_e32 v49, v215
	v_mov_b32_e32 v42, v216
	v_mov_b32_e32 v44, v217
	v_mov_b32_e32 v43, v218
	v_mov_b32_e32 v45, v219
	v_mov_b32_e32 v38, v220
	v_mov_b32_e32 v40, v221
	v_mov_b32_e32 v39, v222
	v_mov_b32_e32 v41, v223
	v_mov_b32_e32 v34, v224
	v_mov_b32_e32 v36, v225
	v_mov_b32_e32 v35, v226
	v_mov_b32_e32 v37, v227
	v_mov_b32_e32 v30, v228
	v_mov_b32_e32 v32, v229
	v_mov_b32_e32 v31, v230
	v_mov_b32_e32 v33, v231
	v_mov_b32_e32 v26, v232
	v_mov_b32_e32 v28, v233
	v_mov_b32_e32 v27, v234
	v_mov_b32_e32 v29, v235
	v_lshrrev_b32_e32 v78, 6, v0
	v_and_b32_e32 v79, 63, v0
	v_mul_u32_u24_e32 v78, 0x2100, v78
	v_mul_u32_u24_e32 v79, 0x84, v79
	v_add_u32_e32 v78, v78, v79
	v_add_u32_e32 v78, 0xa000, v78
	s_lshl_b32 s2, s7, 4
	s_or_b32 s2, s2, s15
	v_cvt_f32_i32_e32 v2, s2
	s_ashr_i32 s3, s2, 31
	s_cmp_gt_i32 s2, 0
	v_div_scale_f32 v3, s[4:5], v77, v77, -v2
	v_rcp_f32_e32 v4, v3
	v_div_scale_f32 v5, vcc, -v2, v77, -v2
	v_fma_f32 v58, -v3, v4, 1.0
	v_fmac_f32_e32 v4, v58, v4
	v_mul_f32_e32 v58, v5, v4
	v_fma_f32 v59, -v3, v58, v5
	v_fmac_f32_e32 v58, v59, v4
	v_fma_f32 v3, -v3, v58, v5
	v_div_fmas_f32 v3, v3, v4, v58
	v_div_fixup_f32 v2, v3, v77, -v2
	v_mul_f32_e64 v2, |v67|, v2
	v_mul_f32_e32 v3, 0x3fb8aa3b, v2
	v_fma_f32 v4, v2, s40, -v3
	v_rndne_f32_e32 v5, v3
	v_fmac_f32_e32 v4, 0x32a5705f, v2
	v_sub_f32_e32 v3, v3, v5
	v_add_f32_e32 v3, v3, v4
	v_cvt_i32_f32_e32 v4, v5
	v_exp_f32_e32 v3, v3
	v_cmp_ngt_f32_e32 vcc, s41, v2
	v_ldexp_f32 v3, v3, v4
	s_nop 0
	v_cndmask_b32_e32 v3, 0, v3, vcc
	v_cmp_nlt_f32_e32 vcc, s42, v2
	s_nop 1
	v_cndmask_b32_e32 v5, v76, v3, vcc
	v_mul_f32_e32 v4, v5, v54
	v_lshl_add_u64 v[2:3], s[2:3], 2, v[24:25]
	ds_write_b32 v78, v4 offset:0
	v_add_f32_e64 v4, v22, |v4|
	s_cbranch_scc0 .LBB0_79
	s_sub_i32 s4, 0, s2
	v_mul_f32_e32 v5, v5, v56
	s_ashr_i32 s5, s4, 31
	v_add_f32_e64 v4, |v5|, v4
	v_lshl_add_u64 v[58:59], s[4:5], 2, v[24:25]
	ds_write_b32 v78, v5 offset:124
